# v34 + P0 rope table: the per-lane inverse-frequency power loop (63 dependent f64 multiplies) is computed once per thread instead of once per table element (same multiplication order, bit-identical val
# speedup vs baseline: 1.0208x; 1.0208x over previous
.LBB0_17:
	v_lshl_or_b32 v1, s90, 9, v0
	s_mov_b32 s0, 0x80000
	v_cmp_gt_i32_e32 vcc, s0, v1
	s_and_saveexec_b64 s[2:3], vcc
	s_cbranch_execz .LBB0_24
	s_add_u32 s4, s50, 0x300000
	s_addc_u32 s5, s51, 0
	s_add_u32 s6, s50, 0x500000
	s_mov_b32 s10, 0xd00ab22c
	s_mov_b32 s12, 0x6dc9c883
	s_mov_b32 s14, 0x54442d18
	s_addc_u32 s7, s51, 0
	s_lshl_b32 s22, s52, 9
	v_cmp_ne_u32_e32 vcc, 0, v196
	s_mov_b64 s[8:9], 0
	s_mov_b32 s11, 0x3febb5fa
	s_mov_b32 s13, 0x3fc45f30
	s_mov_b32 s15, 0xc01921fb
	s_mov_b32 s23, 0x7ffff
	v_mov_b32_e32 v2, v1
	v_mov_b64_e32 v[10:11], 1.0
	s_and_saveexec_b64 s[18:19], vcc
	s_cbranch_execz .Lrope_h2
	s_mov_b64 s[20:21], 0
	v_mov_b32_e32 v3, v196
.Lrope_h1:
	v_add_u32_e32 v3, -1, v3
	v_cmp_eq_u32_e64 s[0:1], 0, v3
	s_or_b64 s[20:21], s[0:1], s[20:21]
	v_mul_f64 v[10:11], v[10:11], s[10:11]
	s_andn2_b64 exec, exec, s[20:21]
	s_cbranch_execnz .Lrope_h1
	s_or_b64 exec, exec, s[20:21]
.Lrope_h2:
	s_or_b64 exec, exec, s[18:19]
	s_branch .LBB0_20

.LBB0_20:
	v_mov_b64_e32 v[4:5], v[10:11]
	s_mov_b64 s[18:19], exec
	s_branch .LBB0_19
